# baseline (speedup 1.0000x reference)
.Lmy_ffn_noprio:
	s_lshl_b32 s6, s6, 13
	s_cmp_lg_u32 0, -1
	s_cselect_b32 s7, 0, 0
	s_add_i32 s10, s7, s6
	s_mov_b64 s[6:7], 0x2000
	s_add_i32 s8, s10, 0x13400
	v_lshl_add_u64 v[24:25], v[180:181], 0, s[6:7]
	s_mov_b32 s9, m0
	s_mov_b32 m0, s8
	s_nop 0
	global_load_lds_dwordx4 v[24:25], off
	s_mov_b32 m0, s9
	s_mov_b64 s[8:9], 0xa000
	v_lshl_add_u64 v[24:25], v[180:181], 0, s[8:9]
	s_add_i32 s8, s10, 0x13800
	s_mov_b32 s9, m0
	s_mov_b32 m0, s8
	s_nop 0
	global_load_lds_dwordx4 v[24:25], off
	s_mov_b32 m0, s9
	s_mov_b64 s[8:9], 0x2400
	s_add_i32 s11, s10, 0x13c00
	v_lshl_add_u64 v[24:25], v[180:181], 0, s[8:9]
	s_mov_b32 s8, m0
	s_mov_b32 m0, s11
	s_nop 0
	global_load_lds_dwordx4 v[24:25], off
	s_mov_b32 m0, s8
	s_mov_b64 s[8:9], 0xa400
	v_lshl_add_u64 v[24:25], v[180:181], 0, s[8:9]
	s_add_i32 s8, s10, 0x14000
	s_mov_b32 s9, m0
	s_mov_b32 m0, s8
	s_nop 0
	global_load_lds_dwordx4 v[24:25], off
	s_mov_b32 m0, s9
	s_mov_b64 s[8:9], 0x2800
	s_add_i32 s11, s10, 0x14400
	v_lshl_add_u64 v[24:25], v[180:181], 0, s[8:9]
	s_mov_b32 s8, m0
	s_mov_b32 m0, s11
	s_nop 0
	global_load_lds_dwordx4 v[24:25], off
	s_mov_b32 m0, s8
	s_mov_b64 s[8:9], 0xa800
	v_lshl_add_u64 v[24:25], v[180:181], 0, s[8:9]
	s_add_i32 s8, s10, 0x14800
	s_mov_b32 s9, m0
	s_mov_b32 m0, s8
	s_nop 0
	global_load_lds_dwordx4 v[24:25], off
	s_mov_b32 m0, s9
	s_mov_b64 s[8:9], 0x2c00
	s_add_i32 s11, s10, 0x14c00
	v_lshl_add_u64 v[24:25], v[180:181], 0, s[8:9]
	s_mov_b32 s8, m0
	s_mov_b32 m0, s11
	s_nop 0
	global_load_lds_dwordx4 v[24:25], off
	s_mov_b32 m0, s8
	s_mov_b64 s[8:9], 0xac00
	v_lshl_add_u64 v[24:25], v[180:181], 0, s[8:9]
	s_add_i32 s9, 0, 0x11400
	v_lshl_add_u32 v19, v37, 2, s9
	s_add_i32 s10, s10, 0x15000
	s_mov_b32 s8, m0
	s_mov_b32 m0, s10
	s_nop 0
	global_load_lds_dwordx4 v[24:25], off
	s_mov_b32 m0, s8
	s_waitcnt vmcnt(8)
	ds_write_b128 v19, v[20:23]
	v_lshrrev_b32_e32 v19, 5, v0
	v_mul_u32_u24_e32 v19, 0x410, v19
	v_and_b32_e32 v18, 0x1f0, v18
	v_add3_u32 v19, 0, v19, v18
	ds_write_b128 v19, v[14:17] offset:512
	v_lshrrev_b32_e32 v14, 5, v186
	v_mul_u32_u24_e32 v14, 0x410, v14
	v_add3_u32 v14, 0, v14, v18
	ds_write_b128 v14, v[6:9] offset:512
	v_lshrrev_b32_e32 v6, 5, v182
	v_mul_u32_u24_e32 v6, 0x410, v6
	v_add3_u32 v6, 0, v6, v18
	s_movk_i32 s10, 0x410
	ds_write_b128 v6, v[2:5] offset:512
	v_lshrrev_b32_e32 v2, 5, v185
	v_mul_u32_u24_e32 v2, 0x410, v2
	v_mad_u32_u24 v189, v205, s10, 0
	v_add3_u32 v2, 0, v2, v18
	v_lshl_add_u32 v202, v208, 4, v189
	ds_write_b128 v2, v[10:13] offset:512
	s_waitcnt lgkmcnt(0)
	s_barrier
	ds_read_b128 v[2:5], v202 offset:512
	ds_read_b128 v[102:105], v202 offset:544
	ds_read_b128 v[6:9], v202 offset:33792
	ds_read_b128 v[106:109], v202 offset:33824
	v_mul_u32_u24_e32 v187, 0x410, v205
	global_load_dwordx4 v[110:113], v[128:129], off
	s_waitcnt vmcnt(8) lgkmcnt(3)
	v_mfma_f32_32x32x16_f16 v[18:33], v[38:41], v[2:5], 0
	ds_read_b128 v[114:117], v202 offset:576
	ds_read_b128 v[118:121], v202 offset:33856
	s_waitcnt lgkmcnt(3)
	v_mfma_f32_32x32x16_f16 v[2:17], v[38:41], v[6:9], 0
	global_load_dwordx4 v[38:41], v[128:129], off offset:1024
	s_waitcnt vmcnt(8)
	v_mfma_f32_32x32x16_f16 v[18:33], v[42:45], v[102:105], v[18:33]
	ds_read_b128 v[102:105], v202 offset:608
	ds_read_b128 v[122:125], v202 offset:33888
	s_waitcnt lgkmcnt(4)
	v_mfma_f32_32x32x16_f16 v[2:17], v[42:45], v[106:109], v[2:17]
	global_load_dwordx4 v[42:45], v[128:129], off offset:2048
	s_waitcnt vmcnt(8) lgkmcnt(3)
	v_mfma_f32_32x32x16_f16 v[18:33], v[46:49], v[114:117], v[18:33]
	ds_read_b128 v[106:109], v202 offset:640
	ds_read_b128 v[114:117], v202 offset:33920
	s_waitcnt lgkmcnt(4)
	v_mfma_f32_32x32x16_f16 v[2:17], v[46:49], v[118:121], v[2:17]
	global_load_dwordx4 v[46:49], v[128:129], off offset:3072
	s_waitcnt vmcnt(8) lgkmcnt(3)
	v_mfma_f32_32x32x16_f16 v[18:33], v[50:53], v[102:105], v[18:33]
	ds_read_b128 v[102:105], v202 offset:672
	ds_read_b128 v[118:121], v202 offset:33952
	s_waitcnt lgkmcnt(4)
	v_mfma_f32_32x32x16_f16 v[2:17], v[50:53], v[122:125], v[2:17]
	s_movk_i32 s8, 0x3000
	v_add_co_u32_e32 v126, vcc, s8, v126
	s_waitcnt vmcnt(7) lgkmcnt(3)
	v_mfma_f32_32x32x16_f16 v[18:33], v[54:57], v[106:109], v[18:33]
	v_addc_co_u32_e32 v127, vcc, 0, v127, vcc
	global_load_dwordx4 v[50:53], v[126:127], off
	ds_read_b128 v[106:109], v202 offset:704
	ds_read_b128 v[122:125], v202 offset:33984
	s_waitcnt lgkmcnt(4)
	v_mfma_f32_32x32x16_f16 v[2:17], v[54:57], v[114:117], v[2:17]
	global_load_dwordx4 v[54:57], v[126:127], off offset:1024
	s_waitcnt vmcnt(8) lgkmcnt(3)
	v_mfma_f32_32x32x16_f16 v[18:33], v[58:61], v[102:105], v[18:33]
	ds_read_b128 v[102:105], v202 offset:736
	ds_read_b128 v[114:117], v202 offset:34016
	s_waitcnt lgkmcnt(4)
	v_mfma_f32_32x32x16_f16 v[2:17], v[58:61], v[118:121], v[2:17]
	global_load_dwordx4 v[58:61], v[126:127], off offset:2048
	s_waitcnt vmcnt(8) lgkmcnt(3)
	v_mfma_f32_32x32x16_f16 v[18:33], v[62:65], v[106:109], v[18:33]
	ds_read_b128 v[106:109], v202 offset:768
	ds_read_b128 v[118:121], v202 offset:34048
	s_waitcnt lgkmcnt(4)
	v_mfma_f32_32x32x16_f16 v[2:17], v[62:65], v[122:125], v[2:17]
	global_load_dwordx4 v[62:65], v[126:127], off offset:3072
	s_waitcnt vmcnt(8) lgkmcnt(3)
	v_mfma_f32_32x32x16_f16 v[18:33], v[98:101], v[102:105], v[18:33]
	ds_read_b128 v[102:105], v202 offset:800
	ds_read_b128 v[122:125], v202 offset:34080
	s_waitcnt lgkmcnt(4)
	v_mfma_f32_32x32x16_f16 v[2:17], v[98:101], v[114:117], v[2:17]
	s_waitcnt vmcnt(7) lgkmcnt(3)
	v_mfma_f32_32x32x16_f16 v[18:33], v[110:113], v[106:109], v[18:33]
	ds_read_b128 v[98:101], v202 offset:832
	ds_read_b128 v[106:109], v202 offset:34112
	s_waitcnt lgkmcnt(4)
	v_mfma_f32_32x32x16_f16 v[2:17], v[110:113], v[118:121], v[2:17]
	s_waitcnt vmcnt(6) lgkmcnt(3)
	v_mfma_f32_32x32x16_f16 v[18:33], v[38:41], v[102:105], v[18:33]
	ds_read_b128 v[102:105], v202 offset:864
	ds_read_b128 v[110:113], v202 offset:34144
	s_waitcnt lgkmcnt(4)
	v_mfma_f32_32x32x16_f16 v[2:17], v[38:41], v[122:125], v[2:17]
	s_waitcnt vmcnt(5) lgkmcnt(3)
	v_mfma_f32_32x32x16_f16 v[18:33], v[42:45], v[98:101], v[18:33]
	ds_read_b128 v[38:41], v202 offset:896
	ds_read_b128 v[98:101], v202 offset:34176
	s_waitcnt lgkmcnt(4)
	v_mfma_f32_32x32x16_f16 v[2:17], v[42:45], v[106:109], v[2:17]
	s_waitcnt vmcnt(4) lgkmcnt(3)
	v_mfma_f32_32x32x16_f16 v[18:33], v[46:49], v[102:105], v[18:33]
	ds_read_b128 v[42:45], v202 offset:928
	ds_read_b128 v[102:105], v202 offset:34208
	s_waitcnt lgkmcnt(4)
	v_mfma_f32_32x32x16_f16 v[2:17], v[46:49], v[110:113], v[2:17]
	s_waitcnt vmcnt(3) lgkmcnt(3)
	v_mfma_f32_32x32x16_f16 v[18:33], v[50:53], v[38:41], v[18:33]
	ds_read_b128 v[38:41], v202 offset:960
	ds_read_b128 v[46:49], v202 offset:34240
	s_waitcnt lgkmcnt(4)
	v_mfma_f32_32x32x16_f16 v[2:17], v[50:53], v[98:101], v[2:17]
	s_waitcnt vmcnt(2) lgkmcnt(3)
	v_mfma_f32_32x32x16_f16 v[18:33], v[54:57], v[42:45], v[18:33]
	ds_read_b128 v[42:45], v202 offset:992
	ds_read_b128 v[50:53], v202 offset:34272
	s_waitcnt lgkmcnt(4)
	v_mfma_f32_32x32x16_f16 v[2:17], v[54:57], v[102:105], v[2:17]
	s_waitcnt vmcnt(1) lgkmcnt(3)
	v_mfma_f32_32x32x16_f16 v[18:33], v[58:61], v[38:41], v[18:33]
	s_waitcnt lgkmcnt(2)
	v_mfma_f32_32x32x16_f16 v[2:17], v[58:61], v[46:49], v[2:17]
	s_waitcnt vmcnt(0) lgkmcnt(1)
	v_mfma_f32_32x32x16_f16 v[18:33], v[62:65], v[42:45], v[18:33]
	s_waitcnt lgkmcnt(0)
	v_mfma_f32_32x32x16_f16 v[2:17], v[62:65], v[50:53], v[2:17]
	v_and_b32_e32 v188, 0xfc, v37
	v_lshl_add_u32 v35, v188, 1, 0
	v_cvt_pk_f16_f32 v39, v92, v93
	v_cvt_pk_f16_f32 v38, v90, v91
	v_mad_u32_u24 v37, v209, s10, v35
	ds_write_b64 v37, v[38:39]
	v_lshrrev_b32_e32 v37, 6, v186
	v_cvt_pk_f16_f32 v39, v96, v97
	v_cvt_pk_f16_f32 v38, v94, v95
	v_mad_u32_u24 v40, v37, s10, v35
	v_lshrrev_b32_e32 v44, 6, v182
	ds_write_b64 v40, v[38:39]
	v_cvt_pk_f16_f32 v39, v88, v89
	v_cvt_pk_f16_f32 v38, v86, v87
	v_mad_u32_u24 v40, v44, s10, v35
	v_lshrrev_b32_e32 v45, 6, v185
	ds_write_b64 v40, v[38:39]
	v_cvt_pk_f16_f32 v39, v84, v85
	v_cvt_pk_f16_f32 v38, v82, v83
	v_mad_u32_u24 v40, v45, s10, v35
	v_lshrrev_b32_e32 v46, 6, v179
	ds_write_b64 v40, v[38:39]
	v_cvt_pk_f16_f32 v39, v80, v81
	v_cvt_pk_f16_f32 v38, v78, v79
	v_mad_u32_u24 v40, v46, s10, v35
	v_lshrrev_b32_e32 v47, 6, v184
	ds_write_b64 v40, v[38:39]
	v_cvt_pk_f16_f32 v39, v76, v77
	v_cvt_pk_f16_f32 v38, v74, v75
	v_mad_u32_u24 v40, v47, s10, v35
	v_lshrrev_b32_e32 v48, 6, v1
	ds_write_b64 v40, v[38:39]
	v_cvt_pk_f16_f32 v39, v72, v73
	v_cvt_pk_f16_f32 v38, v70, v71
	v_mad_u32_u24 v40, v48, s10, v35
	v_lshrrev_b32_e32 v49, 6, v183
	v_lshlrev_b32_e32 v207, 2, v208
	ds_write_b64 v40, v[38:39]
	v_cvt_pk_f16_f32 v39, v68, v69
	v_cvt_pk_f16_f32 v38, v66, v67
	v_mad_u32_u24 v35, v49, s10, v35
	v_lshl_or_b32 v191, v209, 5, v207
	ds_write_b64 v35, v[38:39]
	v_lshl_add_u32 v35, v191, 2, s9
	v_or_b32_e32 v194, 8, v191
	v_or_b32_e32 v200, 16, v191
	v_or_b32_e32 v201, 24, v191
	ds_read_b128 v[50:53], v35
	v_lshl_add_u32 v35, v194, 2, s9
	ds_read_b128 v[54:57], v35
	v_lshl_add_u32 v35, v200, 2, s9
	ds_read_b128 v[58:61], v35
	v_lshl_add_u32 v35, v201, 2, s9
	ds_read_b128 v[62:65], v35
	v_lshl_add_u32 v35, v191, 1, v189
	s_waitcnt lgkmcnt(0)
	s_barrier
	v_add_f32_e32 v18, v50, v18
	v_add_f32_e32 v19, v51, v19
	v_add_f32_e32 v20, v52, v20
	v_add_f32_e32 v21, v53, v21
	v_cvt_pk_f16_f32 v18, v18, v19
	v_cvt_pk_f16_f32 v19, v20, v21
	ds_write_b64 v35, v[18:19] offset:512
	v_add_f32_e32 v2, v50, v2
	v_add_f32_e32 v3, v51, v3
	v_add_f32_e32 v4, v52, v4
	v_add_f32_e32 v5, v53, v5
	v_cvt_pk_f16_f32 v2, v2, v3
	v_cvt_pk_f16_f32 v3, v4, v5
	ds_write_b64 v35, v[2:3] offset:33792
	v_add_f32_e32 v22, v54, v22
	v_add_f32_e32 v23, v55, v23
	v_add_f32_e32 v24, v56, v24
	v_add_f32_e32 v25, v57, v25
	v_cvt_pk_f16_f32 v22, v22, v23
	v_cvt_pk_f16_f32 v23, v24, v25
	ds_write_b64 v35, v[22:23] offset:528
	v_add_f32_e32 v6, v54, v6
	v_add_f32_e32 v7, v55, v7
	v_add_f32_e32 v8, v56, v8
	v_add_f32_e32 v9, v57, v9
	v_cvt_pk_f16_f32 v6, v6, v7
	v_cvt_pk_f16_f32 v7, v8, v9
	ds_write_b64 v35, v[6:7] offset:33808
	v_add_f32_e32 v26, v58, v26
	v_add_f32_e32 v27, v59, v27
	v_add_f32_e32 v28, v60, v28
	v_add_f32_e32 v29, v61, v29
	v_cvt_pk_f16_f32 v26, v26, v27
	v_cvt_pk_f16_f32 v27, v28, v29
	ds_write_b64 v35, v[26:27] offset:544
	v_add_f32_e32 v10, v58, v10
	v_add_f32_e32 v11, v59, v11
	v_add_f32_e32 v12, v60, v12
	v_add_f32_e32 v13, v61, v13
	v_cvt_pk_f16_f32 v10, v10, v11
	v_cvt_pk_f16_f32 v11, v12, v13
	ds_write_b64 v35, v[10:11] offset:33824
	v_add_f32_e32 v30, v62, v30
	v_add_f32_e32 v31, v63, v31
	v_add_f32_e32 v32, v64, v32
	v_add_f32_e32 v33, v65, v33
	v_cvt_pk_f16_f32 v30, v30, v31
	v_cvt_pk_f16_f32 v31, v32, v33
	ds_write_b64 v35, v[30:31] offset:560
	v_add_f32_e32 v14, v62, v14
	v_add_f32_e32 v15, v63, v15
	v_add_f32_e32 v16, v64, v16
	v_add_f32_e32 v17, v65, v17
	v_cvt_pk_f16_f32 v14, v14, v15
	v_cvt_pk_f16_f32 v15, v16, v17
	ds_write_b64 v35, v[14:15] offset:33840
	s_mov_b32 s15, 0x9000
	v_mul_u32_u24_e32 v199, 0x410, v209
	v_mul_u32_u24_e32 v198, 0x410, v37
	v_mul_u32_u24_e32 v197, 0x410, v44
	v_mul_u32_u24_e32 v195, 0x410, v45
	v_mul_u32_u24_e32 v196, 0x410, v46
	v_mul_u32_u24_e32 v193, 0x410, v47
	v_mul_u32_u24_e32 v192, 0x410, v48
	v_mul_u32_u24_e32 v190, 0x410, v49
	v_add_co_u32_e32 v24, vcc, s15, v180
	s_nop 1
	v_addc_co_u32_e32 v25, vcc, 0, v181, vcc
	global_load_dwordx4 v[18:21], v[180:181], off
	global_load_dwordx4 v[102:105], v[24:25], off offset:-4096
	s_mov_b32 s9, 0x8000
	v_add_co_u32_e32 v2, vcc, s9, v180
	s_nop 1
	v_addc_co_u32_e32 v3, vcc, 0, v181, vcc
	global_load_dwordx4 v[106:109], v[180:181], off offset:1024
	global_load_dwordx4 v[110:113], v[2:3], off offset:1024
	global_load_dwordx4 v[122:125], v[180:181], off offset:2048
	global_load_dwordx4 v[126:129], v[2:3], off offset:2048
	global_load_dwordx4 v[130:133], v[180:181], off offset:3072
	global_load_dwordx4 v[134:137], v[2:3], off offset:3072
	v_add_co_u32_e32 v2, vcc, s3, v180
	s_nop 1
	v_addc_co_u32_e32 v3, vcc, 0, v181, vcc
	global_load_dwordx4 v[138:141], v[2:3], off
	global_load_dwordx4 v[142:145], v[24:25], off
	global_load_dwordx4 v[150:153], v[2:3], off offset:1024
	global_load_dwordx4 v[154:157], v[24:25], off offset:1024
	global_load_dwordx4 v[158:161], v[2:3], off offset:2048
	global_load_dwordx4 v[162:165], v[24:25], off offset:2048
	global_load_dwordx4 v[166:169], v[2:3], off offset:3072
	global_load_dwordx4 v[210:213], v[24:25], off offset:3072
	s_waitcnt lgkmcnt(0)
	s_barrier
	ds_read_b128 v[2:5], v202
	ds_read_b128 v[114:117], v202 offset:32
	ds_read_b128 v[6:9], v202 offset:33280
	ds_read_b128 v[146:149], v202 offset:33312
	s_add_i32 s9, 0, 0x13400
	v_add3_u32 v204, s9, v36, v34
	s_waitcnt vmcnt(15) lgkmcnt(3)
	v_mfma_f32_32x32x16_f16 v[50:65], v[18:21], v[2:5], 0
	ds_read_b128 v[170:173], v202 offset:64
	ds_read_b128 v[174:177], v202 offset:33344
	ds_read_b128 v[118:121], v204
	ds_read_b128 v[98:101], v204 offset:1024
	s_waitcnt lgkmcnt(5)
	v_mfma_f32_32x32x16_f16 v[34:49], v[18:21], v[6:9], 0
	s_waitcnt vmcnt(14)
	v_mfma_f32_32x32x16_f16 v[18:33], v[102:105], v[2:5], 0
	v_mfma_f32_32x32x16_f16 v[2:17], v[102:105], v[6:9], 0
	s_waitcnt vmcnt(13)
	v_mfma_f32_32x32x16_f16 v[50:65], v[106:109], v[114:117], v[50:65]
	s_waitcnt lgkmcnt(4)
	v_mfma_f32_32x32x16_f16 v[34:49], v[106:109], v[146:149], v[34:49]
	s_waitcnt vmcnt(12)
	v_mfma_f32_32x32x16_f16 v[18:33], v[110:113], v[114:117], v[18:33]
	ds_read_b128 v[214:217], v202 offset:96
	ds_read_b128 v[218:221], v202 offset:33376
	ds_read_b128 v[114:117], v204 offset:2048
	ds_read_b128 v[102:105], v204 offset:3072
	v_mfma_f32_32x32x16_f16 v[2:17], v[110:113], v[146:149], v[2:17]
	s_waitcnt vmcnt(11) lgkmcnt(7)
	v_mfma_f32_32x32x16_f16 v[50:65], v[122:125], v[170:173], v[50:65]
	s_waitcnt lgkmcnt(6)
	v_mfma_f32_32x32x16_f16 v[34:49], v[122:125], v[174:177], v[34:49]
	s_waitcnt vmcnt(10)
	v_mfma_f32_32x32x16_f16 v[18:33], v[126:129], v[170:173], v[18:33]
	ds_read_b128 v[146:149], v202 offset:128
	ds_read_b128 v[170:173], v202 offset:33408
	ds_read_b128 v[122:125], v204 offset:4096
	ds_read_b128 v[106:109], v204 offset:5120
	v_mfma_f32_32x32x16_f16 v[2:17], v[126:129], v[174:177], v[2:17]
	s_waitcnt vmcnt(9) lgkmcnt(7)
	v_mfma_f32_32x32x16_f16 v[50:65], v[130:133], v[214:217], v[50:65]
	s_waitcnt lgkmcnt(6)
	v_mfma_f32_32x32x16_f16 v[34:49], v[130:133], v[218:221], v[34:49]
	ds_read_b128 v[130:133], v202 offset:160
	ds_read_b128 v[174:177], v202 offset:33440
	ds_read_b128 v[126:129], v204 offset:6144
	ds_read_b128 v[110:113], v204 offset:7168
	s_waitcnt vmcnt(8)
	v_mfma_f32_32x32x16_f16 v[18:33], v[134:137], v[214:217], v[18:33]
	v_mfma_f32_32x32x16_f16 v[2:17], v[134:137], v[218:221], v[2:17]
	v_add_co_u32_e32 v226, vcc, s8, v180
	s_mov_b32 s8, 0xb000
	s_nop 0
	v_addc_co_u32_e32 v227, vcc, 0, v181, vcc
	v_add_co_u32_e32 v228, vcc, s8, v180
	s_waitcnt vmcnt(7) lgkmcnt(7)
	v_mfma_f32_32x32x16_f16 v[50:65], v[138:141], v[146:149], v[50:65]
	v_addc_co_u32_e32 v229, vcc, 0, v181, vcc
	s_waitcnt vmcnt(6)
	v_mfma_f32_32x32x16_f16 v[18:33], v[142:145], v[146:149], v[18:33]
	global_load_dwordx4 v[146:149], v[226:227], off
	global_load_dwordx4 v[134:137], v[228:229], off
	s_waitcnt lgkmcnt(6)
	v_mfma_f32_32x32x16_f16 v[34:49], v[138:141], v[170:173], v[34:49]
	ds_read_b128 v[138:141], v202 offset:192
	ds_read_b128 v[214:217], v202 offset:33472
	v_mfma_f32_32x32x16_f16 v[2:17], v[142:145], v[170:173], v[2:17]
	s_waitcnt vmcnt(7) lgkmcnt(5)
	v_mfma_f32_32x32x16_f16 v[50:65], v[150:153], v[130:133], v[50:65]
	s_waitcnt vmcnt(6)
	v_mfma_f32_32x32x16_f16 v[18:33], v[154:157], v[130:133], v[18:33]
	global_load_dwordx4 v[142:145], v[226:227], off offset:1024
	global_load_dwordx4 v[130:133], v[228:229], off offset:1024
	ds_read_b128 v[218:221], v202 offset:224
	ds_read_b128 v[222:225], v202 offset:33504
	s_waitcnt lgkmcnt(6)
	v_mfma_f32_32x32x16_f16 v[34:49], v[150:153], v[174:177], v[34:49]
	v_mfma_f32_32x32x16_f16 v[2:17], v[154:157], v[174:177], v[2:17]
	s_waitcnt vmcnt(7) lgkmcnt(3)
	v_mfma_f32_32x32x16_f16 v[50:65], v[158:161], v[138:141], v[50:65]
	s_waitcnt vmcnt(6)
	v_mfma_f32_32x32x16_f16 v[18:33], v[162:165], v[138:141], v[18:33]
	global_load_dwordx4 v[150:153], v[226:227], off offset:2048
	global_load_dwordx4 v[138:141], v[228:229], off offset:2048
	ds_read_b128 v[174:177], v202 offset:256
	ds_read_b128 v[170:173], v202 offset:33536
	s_waitcnt lgkmcnt(4)
	v_mfma_f32_32x32x16_f16 v[34:49], v[158:161], v[214:217], v[34:49]
	v_mfma_f32_32x32x16_f16 v[2:17], v[162:165], v[214:217], v[2:17]
	global_load_dwordx4 v[158:161], v[226:227], off offset:3072
	global_load_dwordx4 v[154:157], v[228:229], off offset:3072
	s_waitcnt vmcnt(9) lgkmcnt(3)
	v_mfma_f32_32x32x16_f16 v[50:65], v[166:169], v[218:221], v[50:65]
	s_waitcnt lgkmcnt(2)
	v_mfma_f32_32x32x16_f16 v[34:49], v[166:169], v[222:225], v[34:49]
	ds_read_b128 v[166:169], v202 offset:288
	ds_read_b128 v[162:165], v202 offset:33568
	s_waitcnt vmcnt(8)
	v_mfma_f32_32x32x16_f16 v[18:33], v[210:213], v[218:221], v[18:33]
	v_mfma_f32_32x32x16_f16 v[2:17], v[210:213], v[222:225], v[2:17]
	s_mov_b64 s[8:9], 0x4000
	v_add_u32_e32 v203, 0x140, v202
	v_lshl_add_u64 v[180:181], v[180:181], 0, s[8:9]
	s_mov_b64 s[8:9], 0x8000
	s_mov_b64 s[10:11], 0x1000
	s_mov_b64 s[12:13], 0x9000
	v_mov_b32_e32 v210, v203
